# v86 + static s_setprio 1 for waves 4-7 through the attention tile loop (younger-wave priority raise, no per-segment toggling)
# speedup vs baseline: 1.0014x; 1.0014x over previous
.Lat_setup_done:
	s_barrier
	s_cmp_ge_u32 s68, 0x2000
	s_cbranch_scc0 .Lat_noprio
	s_setprio 1
.Lat_noprio:
	s_cmp_gt_i32 s65, s64
	s_cbranch_scc1 .Lat_tile0
	v_add_u32_e32 v246, s33, v166
	v_add_u32_e32 v247, s33, v168
	v_add_u32_e32 v248, s33, v169
	v_add_u32_e32 v249, s33, v170
	ds_read_b128 v[208:211], v246
	ds_read_b128 v[212:215], v246 offset:8192
	ds_read_b128 v[216:219], v247
	ds_read_b128 v[220:223], v247 offset:8192
	ds_read_b128 v[224:227], v248
	ds_read_b128 v[234:237], v248 offset:8192
	ds_read_b128 v[238:241], v249
	ds_read_b128 v[242:245], v249 offset:8192
	v_add_u32_e32 v246, s33, v251
	v_add_u32_e32 v247, s33, v252
	v_add_u32_e32 v248, s33, v253
	v_add_u32_e32 v249, s33, v254
	s_add_i32 s6, s45, 0
	s_and_b32 s6, s6, 3
	s_lshl_b32 s6, s6, 8
	s_add_i32 s6, s6, 0x10800
	v_add_u32_e32 v152, s6, v164
	ds_read_b128 v[96:99], v152
	ds_read_b128 v[100:103], v152 offset:32
	ds_read_b128 v[80:83], v152 offset:128
	ds_read_b128 v[84:87], v152 offset:160
	ds_read_b128 v[104:107], v152 offset:64
	ds_read_b128 v[108:111], v152 offset:96
	ds_read_b128 v[88:91], v152 offset:192
	ds_read_b128 v[92:95], v152 offset:224
	s_waitcnt lgkmcnt(0)
	v_mfma_f32_32x32x16_bf16 v[96:111], v[208:211], v[112:115], v[96:111]
	ds_read_b128 v[208:211], v246
	v_mfma_f32_32x32x16_bf16 v[80:95], v[212:215], v[112:115], v[80:95]
	ds_read_b128 v[212:215], v246 offset:8192
	v_mfma_f32_32x32x16_bf16 v[96:111], v[216:219], v[116:119], v[96:111]
	ds_read_b128 v[216:219], v247
	v_mfma_f32_32x32x16_bf16 v[80:95], v[220:223], v[116:119], v[80:95]
	ds_read_b128 v[220:223], v247 offset:8192
	v_mfma_f32_32x32x16_bf16 v[96:111], v[224:227], v[120:123], v[96:111]
	ds_read_b128 v[224:227], v248
	v_mfma_f32_32x32x16_bf16 v[80:95], v[234:237], v[120:123], v[80:95]
	ds_read_b128 v[234:237], v248 offset:8192
	v_mfma_f32_32x32x16_bf16 v[96:111], v[238:241], v[124:127], v[96:111]
	ds_read_b128 v[238:241], v249
	v_mfma_f32_32x32x16_bf16 v[80:95], v[242:245], v[124:127], v[80:95]
	ds_read_b128 v[242:245], v249 offset:8192
	s_waitcnt lgkmcnt(7)
	v_mfma_f32_32x32x16_bf16 v[96:111], v[208:211], v[128:131], v[96:111]
	v_add_u32_e32 v246, s42, v166
	v_add_u32_e32 v247, s42, v168
	v_add_u32_e32 v248, s42, v169
	v_add_u32_e32 v249, s42, v170
	ds_read_b128 v[208:211], v246
	s_waitcnt lgkmcnt(7)
	v_mfma_f32_32x32x16_bf16 v[80:95], v[212:215], v[128:131], v[80:95]
	ds_read_b128 v[212:215], v246 offset:8192
	s_waitcnt lgkmcnt(7)
	v_mfma_f32_32x32x16_bf16 v[96:111], v[216:219], v[132:135], v[96:111]
	ds_read_b128 v[216:219], v247
	s_waitcnt lgkmcnt(7)
	v_mfma_f32_32x32x16_bf16 v[80:95], v[220:223], v[132:135], v[80:95]
	ds_read_b128 v[220:223], v247 offset:8192
	s_waitcnt lgkmcnt(7)
	v_mfma_f32_32x32x16_bf16 v[96:111], v[224:227], v[136:139], v[96:111]
	ds_read_b128 v[224:227], v248
	s_waitcnt lgkmcnt(7)
	v_mfma_f32_32x32x16_bf16 v[80:95], v[234:237], v[136:139], v[80:95]
	ds_read_b128 v[234:237], v248 offset:8192
	s_waitcnt lgkmcnt(7)
	v_mfma_f32_32x32x16_bf16 v[96:111], v[238:241], v[140:143], v[96:111]
	ds_read_b128 v[238:241], v249
	s_waitcnt lgkmcnt(7)
	v_mfma_f32_32x32x16_bf16 v[80:95], v[242:245], v[140:143], v[80:95]
	ds_read_b128 v[242:245], v249 offset:8192
	s_add_i32 s6, s65, 63
	s_cmp_gt_i32 s6, s44
	s_cbranch_scc1 .Lat_pmasks
	s_cmp_lt_i32 s65, 0x70
	s_cbranch_scc0 .Lat_pnomasks

.Lat_done:
	s_setprio 0
	s_waitcnt lgkmcnt(0)
	s_waitcnt vmcnt(0)
